# post-PEER norm phase rewritten by hand (two rows in flight, DPP reductions, 8-byte fp8 stores)
# speedup vs baseline: 1.0087x; 1.0041x over previous
.LBB0_1259:
	v_readlane_b32 s8, v252, 0
	v_readlane_b32 s9, v252, 1
	s_cmp_le_i32 s8, s5
	s_cselect_b64 s[6:7], -1, 0
	s_cmp_lt_i32 s5, s9
	v_readlane_b32 s10, v252, 2
	v_readlane_b32 s11, v252, 3
	s_cselect_b64 s[8:9], -1, 0
	s_and_b64 s[10:11], s[6:7], s[8:9]
	s_andn2_b64 vcc, exec, s[10:11]
	s_cbranch_vccnz .LBB0_1329
	v_readfirstlane_b32 s16, v0
	s_lshr_b32 s16, s16, 6
	s_lshl_b32 s17, s2, 3
	s_add_u32 s16, s16, s17
	s_lshl_b32 s17, s82, 3
	s_add_u32 s18, s96, s17
	s_sub_u32 s18, s18, 1
	v_cvt_f32_u32_e32 v136, s17
	v_cvt_f32_u32_e32 v137, s18
	v_rcp_iflag_f32_e32 v136, v136
	s_nop 0
	v_mul_f32_e32 v136, v137, v136
	v_cvt_u32_f32_e32 v136, v136
	s_nop 0
	v_readfirstlane_b32 s19, v136
	s_mul_i32 s12, s19, s17
	s_cmp_gt_u32 s12, s18
	s_cselect_b32 s13, 1, 0
	s_sub_u32 s19, s19, s13
	s_add_u32 s12, s19, 1
	s_mul_i32 s12, s12, s17
	s_cmp_le_u32 s12, s18
	s_cselect_b32 s13, 1, 0
	s_add_u32 s19, s19, s13
	s_mul_i32 s12, s16, s19
	s_cmp_ge_u32 s12, s96
	s_cbranch_scc1 .Lpn_end
	s_add_u32 s13, s12, s19
	s_min_u32 s13, s13, s96
	v_readlane_b32 s4, v252, 4
	v_readlane_b32 s5, v252, 5
	v_readlane_b32 s14, v255, 34
	s_sub_u32 s4, s4, 0x28
	s_subb_u32 s5, s5, 0
	s_load_dwordx2 s[50:51], s[4:5], 0x0
	s_load_dwordx2 s[42:43], s[4:5], 0x8
	s_load_dwordx2 s[4:5], s[4:5], 0x10
	v_and_b32_e32 v2, 63, v0
	v_lshlrev_b32_e32 v3, 4, v2
	v_lshlrev_b32_e32 v160, 5, v2
	v_add_u32_e32 v161, 0x1000, v160
	v_lshlrev_b32_e32 v163, 3, v2
	v_and_b32_e32 v162, 15, v2
	v_mul_u32_u24_e32 v162, 0x11000, v162
	v_cmp_gt_u32_e64 s[54:55], 16, v2
	s_waitcnt lgkmcnt(0)
	s_add_u32 s38, s4, 0x15000000
	s_addc_u32 s39, s5, 0
	s_add_u32 s40, s4, 0x39a00000
	s_addc_u32 s41, s5, 0
	s_cmp_lg_u32 s14, 0
	s_cbranch_scc1 .Lpn_last_setup
	s_add_u32 s42, s4, 0x1b200000
	s_addc_u32 s43, s5, 0
	s_add_u32 s44, s4, 0x12b00000
	s_addc_u32 s45, s5, 0
	s_add_u32 s46, s4, 0x4c000
	s_addc_u32 s47, s5, 0
	v_readlane_b32 s48, v252, 16
	v_readlane_b32 s49, v252, 17
	v_readlane_b32 s50, v252, 18
	v_readlane_b32 s51, v252, 19
	s_add_u32 s48, s48, 0xc000
	s_addc_u32 s49, s49, 0
	s_add_u32 s50, s50, 0x2000
	s_addc_u32 s51, s51, 0
	s_branch .Lpn_setup_done
.Lpn_last_setup:
	v_mov_b32_e32 v136, 0
	global_load_dword v137, v136, s[4:5] offset:96 sc1
	global_load_dwordx4 v[6:9], v160, s[50:51]
	global_load_dwordx4 v[10:13], v160, s[50:51] offset:16
	global_load_dwordx4 v[14:17], v160, s[50:51] offset:2048
	global_load_dwordx4 v[18:21], v160, s[50:51] offset:2064
	global_load_dwordx4 v[22:25], v161, s[50:51]
	global_load_dwordx4 v[26:29], v161, s[50:51] offset:16
	global_load_dwordx4 v[30:33], v161, s[50:51] offset:2048
	global_load_dwordx4 v[34:37], v161, s[50:51] offset:2064
	s_waitcnt vmcnt(0)
	v_cmp_ne_u32_e32 vcc, 0, v137
	s_nop 1
	v_cndmask_b32_e64 v6, v6, 0, vcc
	v_cndmask_b32_e64 v7, v7, 0, vcc
	v_cndmask_b32_e64 v8, v8, 0, vcc
	v_cndmask_b32_e64 v9, v9, 0, vcc
	v_cndmask_b32_e64 v10, v10, 0, vcc
	v_cndmask_b32_e64 v11, v11, 0, vcc
	v_cndmask_b32_e64 v12, v12, 0, vcc
	v_cndmask_b32_e64 v13, v13, 0, vcc
	v_cndmask_b32_e64 v14, v14, 0, vcc
	v_cndmask_b32_e64 v15, v15, 0, vcc
	v_cndmask_b32_e64 v16, v16, 0, vcc
	v_cndmask_b32_e64 v17, v17, 0, vcc
	v_cndmask_b32_e64 v18, v18, 0, vcc
	v_cndmask_b32_e64 v19, v19, 0, vcc
	v_cndmask_b32_e64 v20, v20, 0, vcc
	v_cndmask_b32_e64 v21, v21, 0, vcc
	v_cndmask_b32_e64 v22, v22, 0, vcc
	v_cndmask_b32_e64 v23, v23, 0, vcc
	v_cndmask_b32_e64 v24, v24, 0, vcc
	v_cndmask_b32_e64 v25, v25, 0, vcc
	v_cndmask_b32_e64 v26, v26, 0, vcc
	v_cndmask_b32_e64 v27, v27, 0, vcc
	v_cndmask_b32_e64 v28, v28, 0, vcc
	v_cndmask_b32_e64 v29, v29, 0, vcc
	v_cndmask_b32_e64 v30, v30, 0, vcc
	v_cndmask_b32_e64 v31, v31, 0, vcc
	v_cndmask_b32_e64 v32, v32, 0, vcc
	v_cndmask_b32_e64 v33, v33, 0, vcc
	v_cndmask_b32_e64 v34, v34, 0, vcc
	v_cndmask_b32_e64 v35, v35, 0, vcc
	v_cndmask_b32_e64 v36, v36, 0, vcc
	v_cndmask_b32_e64 v37, v37, 0, vcc
	v_mov_b32_e32 v38, 0
	v_mov_b32_e32 v39, 0
	v_mov_b32_e32 v40, 0
	v_mov_b32_e32 v41, 0
	v_mov_b32_e32 v42, 0
	v_mov_b32_e32 v43, 0
	v_mov_b32_e32 v44, 0
	v_mov_b32_e32 v45, 0
	v_mov_b32_e32 v46, 0
	v_mov_b32_e32 v47, 0
	v_mov_b32_e32 v48, 0
	v_mov_b32_e32 v49, 0
	v_mov_b32_e32 v50, 0
	v_mov_b32_e32 v51, 0
	v_mov_b32_e32 v52, 0
	v_mov_b32_e32 v53, 0
	v_mov_b32_e32 v54, 0
	v_mov_b32_e32 v55, 0
	v_mov_b32_e32 v56, 0
	v_mov_b32_e32 v57, 0
	v_mov_b32_e32 v58, 0
	v_mov_b32_e32 v59, 0
	v_mov_b32_e32 v60, 0
	v_mov_b32_e32 v61, 0
	v_mov_b32_e32 v62, 0
	v_mov_b32_e32 v63, 0
	v_mov_b32_e32 v64, 0
	v_mov_b32_e32 v65, 0
	v_mov_b32_e32 v66, 0
	v_mov_b32_e32 v67, 0
	v_mov_b32_e32 v68, 0
	v_mov_b32_e32 v69, 0
.Lpn_setup_done:
	s_mov_b32 s15, -1
	s_lshl_b32 s16, s12, 12
	s_add_u32 s52, s38, s16
	s_addc_u32 s53, s39, 0
	global_load_dwordx4 v[102:105], v3, s[52:53]
	global_load_dwordx4 v[106:109], v3, s[52:53] offset:1024
	global_load_dwordx4 v[110:113], v3, s[52:53] offset:2048
	global_load_dwordx4 v[114:117], v3, s[52:53] offset:3072
	s_lshl_b32 s16, s12, 2
	s_add_u32 s52, s40, s16
	s_addc_u32 s53, s41, 0
	global_load_dword v134, v162, s[52:53]
	s_add_u32 s18, s12, 1
	s_min_u32 s18, s18, s13
	s_sub_u32 s19, s13, 1
	s_min_u32 s18, s18, s19
	s_lshl_b32 s16, s18, 12
	s_add_u32 s52, s38, s16
	s_addc_u32 s53, s39, 0
	global_load_dwordx4 v[118:121], v3, s[52:53]
	global_load_dwordx4 v[122:125], v3, s[52:53] offset:1024
	global_load_dwordx4 v[126:129], v3, s[52:53] offset:2048
	global_load_dwordx4 v[130:133], v3, s[52:53] offset:3072
	s_lshl_b32 s16, s18, 2
	s_add_u32 s52, s40, s16
	s_addc_u32 s53, s41, 0
	global_load_dword v135, v162, s[52:53]
	s_cmp_lg_u32 s14, 0
	s_cbranch_scc1 .Lpn_mod_ok_a
	s_lshr_b32 s16, s12, 12
	s_cmp_lt_u32 s12, 0x4000
	s_cselect_b32 s16, s16, 4
	s_cmp_eq_u32 s16, s15
	s_cbranch_scc1 .Lpn_mod_ok_a
	s_mov_b32 s15, s16
	s_mul_i32 s16, s16, 0xc000
	s_add_u32 s52, s46, s16
	s_addc_u32 s53, s47, 0
	s_add_u32 s10, s52, 0x2000
	s_addc_u32 s11, s53, 0
	s_add_u32 s16, s48, 0x2000
	s_addc_u32 s17, s49, 0
	global_load_dwordx4 v[6:9], v160, s[10:11]
	global_load_dwordx4 v[70:73], v160, s[16:17]
	global_load_dwordx4 v[38:41], v160, s[52:53]
	global_load_dwordx4 v[10:13], v160, s[10:11] offset:16
	global_load_dwordx4 v[74:77], v160, s[16:17] offset:16
	global_load_dwordx4 v[42:45], v160, s[52:53] offset:16
	global_load_dwordx4 v[14:17], v160, s[10:11] offset:2048
	global_load_dwordx4 v[78:81], v160, s[16:17] offset:2048
	global_load_dwordx4 v[46:49], v160, s[52:53] offset:2048
	global_load_dwordx4 v[18:21], v160, s[10:11] offset:2064
	global_load_dwordx4 v[82:85], v160, s[16:17] offset:2064
	global_load_dwordx4 v[50:53], v160, s[52:53] offset:2064
	global_load_dwordx4 v[22:25], v161, s[10:11]
	global_load_dwordx4 v[86:89], v161, s[16:17]
	global_load_dwordx4 v[54:57], v161, s[52:53]
	global_load_dwordx4 v[26:29], v161, s[10:11] offset:16
	global_load_dwordx4 v[90:93], v161, s[16:17] offset:16
	global_load_dwordx4 v[58:61], v161, s[52:53] offset:16
	global_load_dwordx4 v[30:33], v161, s[10:11] offset:2048
	global_load_dwordx4 v[94:97], v161, s[16:17] offset:2048
	global_load_dwordx4 v[62:65], v161, s[52:53] offset:2048
	global_load_dwordx4 v[34:37], v161, s[10:11] offset:2064
	global_load_dwordx4 v[98:101], v161, s[16:17] offset:2064
	global_load_dwordx4 v[66:69], v161, s[52:53] offset:2064
	s_waitcnt vmcnt(0)
	v_pk_add_f32 v[6:7], v[6:7], v[70:71]
	v_pk_add_f32 v[6:7], v[6:7], 1.0 op_sel_hi:[1,0]
	v_pk_add_f32 v[8:9], v[8:9], v[72:73]
	v_pk_add_f32 v[8:9], v[8:9], 1.0 op_sel_hi:[1,0]
	v_pk_add_f32 v[10:11], v[10:11], v[74:75]
	v_pk_add_f32 v[10:11], v[10:11], 1.0 op_sel_hi:[1,0]
	v_pk_add_f32 v[12:13], v[12:13], v[76:77]
	v_pk_add_f32 v[12:13], v[12:13], 1.0 op_sel_hi:[1,0]
	v_pk_add_f32 v[14:15], v[14:15], v[78:79]
	v_pk_add_f32 v[14:15], v[14:15], 1.0 op_sel_hi:[1,0]
	v_pk_add_f32 v[16:17], v[16:17], v[80:81]
	v_pk_add_f32 v[16:17], v[16:17], 1.0 op_sel_hi:[1,0]
	v_pk_add_f32 v[18:19], v[18:19], v[82:83]
	v_pk_add_f32 v[18:19], v[18:19], 1.0 op_sel_hi:[1,0]
	v_pk_add_f32 v[20:21], v[20:21], v[84:85]
	v_pk_add_f32 v[20:21], v[20:21], 1.0 op_sel_hi:[1,0]
	v_pk_add_f32 v[22:23], v[22:23], v[86:87]
	v_pk_add_f32 v[22:23], v[22:23], 1.0 op_sel_hi:[1,0]
	v_pk_add_f32 v[24:25], v[24:25], v[88:89]
	v_pk_add_f32 v[24:25], v[24:25], 1.0 op_sel_hi:[1,0]
	v_pk_add_f32 v[26:27], v[26:27], v[90:91]
	v_pk_add_f32 v[26:27], v[26:27], 1.0 op_sel_hi:[1,0]
	v_pk_add_f32 v[28:29], v[28:29], v[92:93]
	v_pk_add_f32 v[28:29], v[28:29], 1.0 op_sel_hi:[1,0]
	v_pk_add_f32 v[30:31], v[30:31], v[94:95]
	v_pk_add_f32 v[30:31], v[30:31], 1.0 op_sel_hi:[1,0]
	v_pk_add_f32 v[32:33], v[32:33], v[96:97]
	v_pk_add_f32 v[32:33], v[32:33], 1.0 op_sel_hi:[1,0]
	v_pk_add_f32 v[34:35], v[34:35], v[98:99]
	v_pk_add_f32 v[34:35], v[34:35], 1.0 op_sel_hi:[1,0]
	v_pk_add_f32 v[36:37], v[36:37], v[100:101]
	v_pk_add_f32 v[36:37], v[36:37], 1.0 op_sel_hi:[1,0]
	global_load_dwordx4 v[70:73], v160, s[50:51]
	global_load_dwordx4 v[74:77], v160, s[50:51] offset:16
	global_load_dwordx4 v[78:81], v160, s[50:51] offset:2048
	global_load_dwordx4 v[82:85], v160, s[50:51] offset:2064
	global_load_dwordx4 v[86:89], v161, s[50:51]
	global_load_dwordx4 v[90:93], v161, s[50:51] offset:16
	global_load_dwordx4 v[94:97], v161, s[50:51] offset:2048
	global_load_dwordx4 v[98:101], v161, s[50:51] offset:2064
	s_waitcnt vmcnt(0)
	v_pk_mul_f32 v[6:7], v[70:71], v[6:7]
	v_pk_mul_f32 v[8:9], v[72:73], v[8:9]
	v_pk_mul_f32 v[10:11], v[74:75], v[10:11]
	v_pk_mul_f32 v[12:13], v[76:77], v[12:13]
	v_pk_mul_f32 v[14:15], v[78:79], v[14:15]
	v_pk_mul_f32 v[16:17], v[80:81], v[16:17]
	v_pk_mul_f32 v[18:19], v[82:83], v[18:19]
	v_pk_mul_f32 v[20:21], v[84:85], v[20:21]
	v_pk_mul_f32 v[22:23], v[86:87], v[22:23]
	v_pk_mul_f32 v[24:25], v[88:89], v[24:25]
	v_pk_mul_f32 v[26:27], v[90:91], v[26:27]
	v_pk_mul_f32 v[28:29], v[92:93], v[28:29]
	v_pk_mul_f32 v[30:31], v[94:95], v[30:31]
	v_pk_mul_f32 v[32:33], v[96:97], v[32:33]
	v_pk_mul_f32 v[34:35], v[98:99], v[34:35]
	v_pk_mul_f32 v[36:37], v[100:101], v[36:37]
	global_load_dwordx4 v[70:73], v160, s[48:49]
	global_load_dwordx4 v[74:77], v160, s[48:49] offset:16
	global_load_dwordx4 v[78:81], v160, s[48:49] offset:2048
	global_load_dwordx4 v[82:85], v160, s[48:49] offset:2064
	global_load_dwordx4 v[86:89], v161, s[48:49]
	global_load_dwordx4 v[90:93], v161, s[48:49] offset:16
	global_load_dwordx4 v[94:97], v161, s[48:49] offset:2048
	global_load_dwordx4 v[98:101], v161, s[48:49] offset:2064
	s_waitcnt vmcnt(0)
	v_pk_add_f32 v[38:39], v[38:39], v[70:71]
	v_pk_add_f32 v[40:41], v[40:41], v[72:73]
	v_pk_add_f32 v[42:43], v[42:43], v[74:75]
	v_pk_add_f32 v[44:45], v[44:45], v[76:77]
	v_pk_add_f32 v[46:47], v[46:47], v[78:79]
	v_pk_add_f32 v[48:49], v[48:49], v[80:81]
	v_pk_add_f32 v[50:51], v[50:51], v[82:83]
	v_pk_add_f32 v[52:53], v[52:53], v[84:85]
	v_pk_add_f32 v[54:55], v[54:55], v[86:87]
	v_pk_add_f32 v[56:57], v[56:57], v[88:89]
	v_pk_add_f32 v[58:59], v[58:59], v[90:91]
	v_pk_add_f32 v[60:61], v[60:61], v[92:93]
	v_pk_add_f32 v[62:63], v[62:63], v[94:95]
	v_pk_add_f32 v[64:65], v[64:65], v[96:97]
	v_pk_add_f32 v[66:67], v[66:67], v[98:99]
	v_pk_add_f32 v[68:69], v[68:69], v[100:101]
.Lpn_mod_ok_a:
	s_waitcnt vmcnt(5)
	v_cndmask_b32_e64 v136, 0, v134, s[54:55]
	s_nop 1
	v_add_f32_dpp v136, v136, v136 quad_perm:[1,0,3,2] row_mask:0xf bank_mask:0xf bound_ctrl:1
	s_nop 1
	v_add_f32_dpp v136, v136, v136 quad_perm:[2,3,0,1] row_mask:0xf bank_mask:0xf bound_ctrl:1
	s_nop 1
	v_add_f32_dpp v136, v136, v136 row_half_mirror row_mask:0xf bank_mask:0xf bound_ctrl:1
	s_nop 1
	v_add_f32_dpp v136, v136, v136 row_mirror row_mask:0xf bank_mask:0xf bound_ctrl:1
	s_nop 0
	v_readlane_b32 s16, v136, 0
	s_mov_b32 s17, 0x800000
	s_nop 1
	v_mov_b32_e32 v136, s16
	v_fmamk_f32 v136, v136, 0x3a000000, v212
	v_mul_f32_e32 v137, 0x4b800000, v136
	v_cmp_gt_f32_e32 vcc, s17, v136
	s_nop 1
	v_cndmask_b32_e32 v136, v136, v137, vcc
	v_rsq_f32_e32 v136, v136
	s_nop 0
	v_mul_f32_e32 v137, 0x45800000, v136
	v_cndmask_b32_e32 v136, v136, v137, vcc
	v_mov_b32_e32 v137, v136
	v_lshlrev_b32_e32 v70, 16, v102
	v_and_b32_e32 v71, 0xffff0000, v102
	v_lshlrev_b32_e32 v72, 16, v103
	v_and_b32_e32 v73, 0xffff0000, v103
	v_lshlrev_b32_e32 v74, 16, v104
	v_and_b32_e32 v75, 0xffff0000, v104
	v_lshlrev_b32_e32 v76, 16, v105
	v_and_b32_e32 v77, 0xffff0000, v105
	v_lshlrev_b32_e32 v78, 16, v106
	v_and_b32_e32 v79, 0xffff0000, v106
	v_lshlrev_b32_e32 v80, 16, v107
	v_and_b32_e32 v81, 0xffff0000, v107
	v_lshlrev_b32_e32 v82, 16, v108
	v_and_b32_e32 v83, 0xffff0000, v108
	v_lshlrev_b32_e32 v84, 16, v109
	v_and_b32_e32 v85, 0xffff0000, v109
	v_lshlrev_b32_e32 v86, 16, v110
	v_and_b32_e32 v87, 0xffff0000, v110
	v_lshlrev_b32_e32 v88, 16, v111
	v_and_b32_e32 v89, 0xffff0000, v111
	v_lshlrev_b32_e32 v90, 16, v112
	v_and_b32_e32 v91, 0xffff0000, v112
	v_lshlrev_b32_e32 v92, 16, v113
	v_and_b32_e32 v93, 0xffff0000, v113
	v_lshlrev_b32_e32 v94, 16, v114
	v_and_b32_e32 v95, 0xffff0000, v114
	v_lshlrev_b32_e32 v96, 16, v115
	v_and_b32_e32 v97, 0xffff0000, v115
	v_lshlrev_b32_e32 v98, 16, v116
	v_and_b32_e32 v99, 0xffff0000, v116
	v_lshlrev_b32_e32 v100, 16, v117
	v_and_b32_e32 v101, 0xffff0000, v117
	s_add_u32 s18, s12, 2
	s_sub_u32 s19, s13, 1
	s_min_u32 s18, s18, s19
	s_lshl_b32 s16, s18, 12
	s_add_u32 s52, s38, s16
	s_addc_u32 s53, s39, 0
	global_load_dwordx4 v[102:105], v3, s[52:53]
	global_load_dwordx4 v[106:109], v3, s[52:53] offset:1024
	global_load_dwordx4 v[110:113], v3, s[52:53] offset:2048
	global_load_dwordx4 v[114:117], v3, s[52:53] offset:3072
	s_lshl_b32 s16, s18, 2
	s_add_u32 s52, s40, s16
	s_addc_u32 s53, s41, 0
	global_load_dword v134, v162, s[52:53]
	v_pk_mul_f32 v[70:71], v[70:71], v[136:137]
	v_pk_mul_f32 v[72:73], v[72:73], v[136:137]
	v_pk_mul_f32 v[74:75], v[74:75], v[136:137]
	v_pk_mul_f32 v[76:77], v[76:77], v[136:137]
	v_pk_mul_f32 v[78:79], v[78:79], v[136:137]
	v_pk_mul_f32 v[80:81], v[80:81], v[136:137]
	v_pk_mul_f32 v[82:83], v[82:83], v[136:137]
	v_pk_mul_f32 v[84:85], v[84:85], v[136:137]
	v_pk_mul_f32 v[86:87], v[86:87], v[136:137]
	v_pk_mul_f32 v[88:89], v[88:89], v[136:137]
	v_pk_mul_f32 v[90:91], v[90:91], v[136:137]
	v_pk_mul_f32 v[92:93], v[92:93], v[136:137]
	v_pk_mul_f32 v[94:95], v[94:95], v[136:137]
	v_pk_mul_f32 v[96:97], v[96:97], v[136:137]
	v_pk_mul_f32 v[98:99], v[98:99], v[136:137]
	v_pk_mul_f32 v[100:101], v[100:101], v[136:137]
	v_pk_fma_f32 v[70:71], v[70:71], v[6:7], v[38:39]
	v_pk_fma_f32 v[72:73], v[72:73], v[8:9], v[40:41]
	v_pk_fma_f32 v[74:75], v[74:75], v[10:11], v[42:43]
	v_pk_fma_f32 v[76:77], v[76:77], v[12:13], v[44:45]
	v_pk_fma_f32 v[78:79], v[78:79], v[14:15], v[46:47]
	v_pk_fma_f32 v[80:81], v[80:81], v[16:17], v[48:49]
	v_pk_fma_f32 v[82:83], v[82:83], v[18:19], v[50:51]
	v_pk_fma_f32 v[84:85], v[84:85], v[20:21], v[52:53]
	v_pk_fma_f32 v[86:87], v[86:87], v[22:23], v[54:55]
	v_pk_fma_f32 v[88:89], v[88:89], v[24:25], v[56:57]
	v_pk_fma_f32 v[90:91], v[90:91], v[26:27], v[58:59]
	v_pk_fma_f32 v[92:93], v[92:93], v[28:29], v[60:61]
	v_pk_fma_f32 v[94:95], v[94:95], v[30:31], v[62:63]
	v_pk_fma_f32 v[96:97], v[96:97], v[32:33], v[64:65]
	v_pk_fma_f32 v[98:99], v[98:99], v[34:35], v[66:67]
	v_pk_fma_f32 v[100:101], v[100:101], v[36:37], v[68:69]
	s_cmp_lg_u32 s14, 0
	s_cbranch_scc1 .Lpn_out_a
	v_max3_f32 v138, |v70|, |v71|, |v72|
	v_max3_f32 v139, |v74|, |v75|, |v76|
	v_max3_f32 v140, |v78|, |v79|, |v80|
	v_max3_f32 v141, |v82|, |v83|, |v84|
	v_max3_f32 v142, |v86|, |v87|, |v88|
	v_max3_f32 v143, |v90|, |v91|, |v92|
	v_max3_f32 v144, |v94|, |v95|, |v96|
	v_max3_f32 v145, |v98|, |v99|, |v100|
	v_max_f32_e64 v138, v138, |v73|
	v_max_f32_e64 v139, v139, |v77|
	v_max_f32_e64 v140, v140, |v81|
	v_max_f32_e64 v141, v141, |v85|
	v_max_f32_e64 v142, v142, |v89|
	v_max_f32_e64 v143, v143, |v93|
	v_max_f32_e64 v144, v144, |v97|
	v_max_f32_e64 v145, v145, |v101|
	v_max3_f32 v138, v138, v139, v140
	v_max3_f32 v141, v141, v142, v143
	v_max3_f32 v138, v138, v141, v144
	v_max_f32_e32 v138, v138, v145
	s_nop 1
	v_mov_b32_dpp v139, v138 quad_perm:[1,0,3,2] row_mask:0xf bank_mask:0xf bound_ctrl:1
	v_max_f32_e32 v138, v138, v139
	s_nop 1
	v_mov_b32_dpp v139, v138 quad_perm:[2,3,0,1] row_mask:0xf bank_mask:0xf bound_ctrl:1
	v_max_f32_e32 v138, v138, v139
	s_nop 1
	v_mov_b32_dpp v139, v138 row_half_mirror row_mask:0xf bank_mask:0xf bound_ctrl:1
	v_max_f32_e32 v138, v138, v139
	s_nop 1
	v_mov_b32_dpp v139, v138 row_mirror row_mask:0xf bank_mask:0xf bound_ctrl:1
	v_max_f32_e32 v138, v138, v139
	v_mov_b32_e32 v139, v138
	s_nop 1
	v_permlane16_swap_b32_e32 v138, v139
	v_max_f32_e32 v138, v138, v139
	v_mov_b32_e32 v139, v138
	s_nop 1
	v_permlane32_swap_b32_e32 v138, v139
	v_max_f32_e32 v138, v138, v139
	v_div_scale_f32 v140, s[100:101], v138, v138, s95
	v_rcp_f32_e32 v142, v140
	v_div_scale_f32 v141, vcc, s95, v138, s95
	v_fma_f32 v143, -v140, v142, 1.0
	v_fmac_f32_e32 v142, v143, v142
	v_mul_f32_e32 v143, v141, v142
	v_fma_f32 v144, -v140, v143, v141
	v_fmac_f32_e32 v143, v144, v142
	v_fma_f32 v140, -v140, v143, v141
	v_div_fmas_f32 v140, v140, v142, v143
	v_div_fixup_f32 v140, v140, v138, s95
	v_cmp_lt_f32_e32 vcc, 0, v138
	v_mul_f32_e32 v141, 0x3b124925, v138
	v_mov_b32_e32 v143, 0
	v_cndmask_b32_e32 v142, 0, v140, vcc
	s_lshl_b32 s16, s12, 2
	s_add_u32 s52, s44, s16
	s_addc_u32 s53, s45, 0
	s_mov_b64 exec, 1
	global_store_dword v143, v141, s[52:53]
	s_mov_b64 exec, -1
	v_pk_mul_f32 v[70:71], v[70:71], v[142:143] op_sel_hi:[1,0]
	v_pk_mul_f32 v[72:73], v[72:73], v[142:143] op_sel_hi:[1,0]
	v_pk_mul_f32 v[74:75], v[74:75], v[142:143] op_sel_hi:[1,0]
	v_pk_mul_f32 v[76:77], v[76:77], v[142:143] op_sel_hi:[1,0]
	v_pk_mul_f32 v[78:79], v[78:79], v[142:143] op_sel_hi:[1,0]
	v_pk_mul_f32 v[80:81], v[80:81], v[142:143] op_sel_hi:[1,0]
	v_pk_mul_f32 v[82:83], v[82:83], v[142:143] op_sel_hi:[1,0]
	v_pk_mul_f32 v[84:85], v[84:85], v[142:143] op_sel_hi:[1,0]
	v_pk_mul_f32 v[86:87], v[86:87], v[142:143] op_sel_hi:[1,0]
	v_pk_mul_f32 v[88:89], v[88:89], v[142:143] op_sel_hi:[1,0]
	v_pk_mul_f32 v[90:91], v[90:91], v[142:143] op_sel_hi:[1,0]
	v_pk_mul_f32 v[92:93], v[92:93], v[142:143] op_sel_hi:[1,0]
	v_pk_mul_f32 v[94:95], v[94:95], v[142:143] op_sel_hi:[1,0]
	v_pk_mul_f32 v[96:97], v[96:97], v[142:143] op_sel_hi:[1,0]
	v_pk_mul_f32 v[98:99], v[98:99], v[142:143] op_sel_hi:[1,0]
	v_pk_mul_f32 v[100:101], v[100:101], v[142:143] op_sel_hi:[1,0]
	v_mov_b32_e32 v146, 0
	v_mov_b32_e32 v147, 0
	v_mov_b32_e32 v148, 0
	v_mov_b32_e32 v149, 0
	v_mov_b32_e32 v150, 0
	v_mov_b32_e32 v151, 0
	v_mov_b32_e32 v152, 0
	v_mov_b32_e32 v153, 0
	v_cvt_pk_fp8_f32 v146, v70, v71
	v_cvt_pk_fp8_f32 v147, v74, v75
	v_cvt_pk_fp8_f32 v148, v78, v79
	v_cvt_pk_fp8_f32 v149, v82, v83
	v_cvt_pk_fp8_f32 v150, v86, v87
	v_cvt_pk_fp8_f32 v151, v90, v91
	v_cvt_pk_fp8_f32 v152, v94, v95
	v_cvt_pk_fp8_f32 v153, v98, v99
	v_cvt_pk_fp8_f32 v146, v72, v73 op_sel:[0,0,1]
	v_cvt_pk_fp8_f32 v147, v76, v77 op_sel:[0,0,1]
	v_cvt_pk_fp8_f32 v148, v80, v81 op_sel:[0,0,1]
	v_cvt_pk_fp8_f32 v149, v84, v85 op_sel:[0,0,1]
	v_cvt_pk_fp8_f32 v150, v88, v89 op_sel:[0,0,1]
	v_cvt_pk_fp8_f32 v151, v92, v93 op_sel:[0,0,1]
	v_cvt_pk_fp8_f32 v152, v96, v97 op_sel:[0,0,1]
	v_cvt_pk_fp8_f32 v153, v100, v101 op_sel:[0,0,1]
	s_lshl_b32 s16, s12, 11
	s_add_u32 s52, s42, s16
	s_addc_u32 s53, s43, 0
	global_store_dwordx2 v163, v[146:147], s[52:53]
	global_store_dwordx2 v163, v[148:149], s[52:53] offset:512
	global_store_dwordx2 v163, v[150:151], s[52:53] offset:1024
	global_store_dwordx2 v163, v[152:153], s[52:53] offset:1536
	s_branch .Lpn_next_a
.Lpn_out_a:
	s_lshl_b32 s16, s12, 13
	s_add_u32 s52, s42, s16
	s_addc_u32 s53, s43, 0
	global_store_dwordx4 v160, v[70:73], s[52:53]
	global_store_dwordx4 v160, v[74:77], s[52:53] offset:16
	global_store_dwordx4 v160, v[78:81], s[52:53] offset:2048
	global_store_dwordx4 v160, v[82:85], s[52:53] offset:2064
	global_store_dwordx4 v161, v[86:89], s[52:53]
	global_store_dwordx4 v161, v[90:93], s[52:53] offset:16
	global_store_dwordx4 v161, v[94:97], s[52:53] offset:2048
	global_store_dwordx4 v161, v[98:101], s[52:53] offset:2064
.Lpn_next_a:
	s_add_u32 s12, s12, 1
	s_cmp_ge_u32 s12, s13
	s_cbranch_scc1 .Lpn_end
.Lpn_loop:
	s_cmp_lg_u32 s14, 0
	s_cbranch_scc1 .Lpn_mod_ok_b
	s_lshr_b32 s16, s12, 12
	s_cmp_lt_u32 s12, 0x4000
	s_cselect_b32 s16, s16, 4
	s_cmp_eq_u32 s16, s15
	s_cbranch_scc1 .Lpn_mod_ok_b
	s_mov_b32 s15, s16
	s_mul_i32 s16, s16, 0xc000
	s_add_u32 s52, s46, s16
	s_addc_u32 s53, s47, 0
	s_add_u32 s10, s52, 0x2000
	s_addc_u32 s11, s53, 0
	s_add_u32 s16, s48, 0x2000
	s_addc_u32 s17, s49, 0
	global_load_dwordx4 v[6:9], v160, s[10:11]
	global_load_dwordx4 v[70:73], v160, s[16:17]
	global_load_dwordx4 v[38:41], v160, s[52:53]
	global_load_dwordx4 v[10:13], v160, s[10:11] offset:16
	global_load_dwordx4 v[74:77], v160, s[16:17] offset:16
	global_load_dwordx4 v[42:45], v160, s[52:53] offset:16
	global_load_dwordx4 v[14:17], v160, s[10:11] offset:2048
	global_load_dwordx4 v[78:81], v160, s[16:17] offset:2048
	global_load_dwordx4 v[46:49], v160, s[52:53] offset:2048
	global_load_dwordx4 v[18:21], v160, s[10:11] offset:2064
	global_load_dwordx4 v[82:85], v160, s[16:17] offset:2064
	global_load_dwordx4 v[50:53], v160, s[52:53] offset:2064
	global_load_dwordx4 v[22:25], v161, s[10:11]
	global_load_dwordx4 v[86:89], v161, s[16:17]
	global_load_dwordx4 v[54:57], v161, s[52:53]
	global_load_dwordx4 v[26:29], v161, s[10:11] offset:16
	global_load_dwordx4 v[90:93], v161, s[16:17] offset:16
	global_load_dwordx4 v[58:61], v161, s[52:53] offset:16
	global_load_dwordx4 v[30:33], v161, s[10:11] offset:2048
	global_load_dwordx4 v[94:97], v161, s[16:17] offset:2048
	global_load_dwordx4 v[62:65], v161, s[52:53] offset:2048
	global_load_dwordx4 v[34:37], v161, s[10:11] offset:2064
	global_load_dwordx4 v[98:101], v161, s[16:17] offset:2064
	global_load_dwordx4 v[66:69], v161, s[52:53] offset:2064
	s_waitcnt vmcnt(0)
	v_pk_add_f32 v[6:7], v[6:7], v[70:71]
	v_pk_add_f32 v[6:7], v[6:7], 1.0 op_sel_hi:[1,0]
	v_pk_add_f32 v[8:9], v[8:9], v[72:73]
	v_pk_add_f32 v[8:9], v[8:9], 1.0 op_sel_hi:[1,0]
	v_pk_add_f32 v[10:11], v[10:11], v[74:75]
	v_pk_add_f32 v[10:11], v[10:11], 1.0 op_sel_hi:[1,0]
	v_pk_add_f32 v[12:13], v[12:13], v[76:77]
	v_pk_add_f32 v[12:13], v[12:13], 1.0 op_sel_hi:[1,0]
	v_pk_add_f32 v[14:15], v[14:15], v[78:79]
	v_pk_add_f32 v[14:15], v[14:15], 1.0 op_sel_hi:[1,0]
	v_pk_add_f32 v[16:17], v[16:17], v[80:81]
	v_pk_add_f32 v[16:17], v[16:17], 1.0 op_sel_hi:[1,0]
	v_pk_add_f32 v[18:19], v[18:19], v[82:83]
	v_pk_add_f32 v[18:19], v[18:19], 1.0 op_sel_hi:[1,0]
	v_pk_add_f32 v[20:21], v[20:21], v[84:85]
	v_pk_add_f32 v[20:21], v[20:21], 1.0 op_sel_hi:[1,0]
	v_pk_add_f32 v[22:23], v[22:23], v[86:87]
	v_pk_add_f32 v[22:23], v[22:23], 1.0 op_sel_hi:[1,0]
	v_pk_add_f32 v[24:25], v[24:25], v[88:89]
	v_pk_add_f32 v[24:25], v[24:25], 1.0 op_sel_hi:[1,0]
	v_pk_add_f32 v[26:27], v[26:27], v[90:91]
	v_pk_add_f32 v[26:27], v[26:27], 1.0 op_sel_hi:[1,0]
	v_pk_add_f32 v[28:29], v[28:29], v[92:93]
	v_pk_add_f32 v[28:29], v[28:29], 1.0 op_sel_hi:[1,0]
	v_pk_add_f32 v[30:31], v[30:31], v[94:95]
	v_pk_add_f32 v[30:31], v[30:31], 1.0 op_sel_hi:[1,0]
	v_pk_add_f32 v[32:33], v[32:33], v[96:97]
	v_pk_add_f32 v[32:33], v[32:33], 1.0 op_sel_hi:[1,0]
	v_pk_add_f32 v[34:35], v[34:35], v[98:99]
	v_pk_add_f32 v[34:35], v[34:35], 1.0 op_sel_hi:[1,0]
	v_pk_add_f32 v[36:37], v[36:37], v[100:101]
	v_pk_add_f32 v[36:37], v[36:37], 1.0 op_sel_hi:[1,0]
	global_load_dwordx4 v[70:73], v160, s[50:51]
	global_load_dwordx4 v[74:77], v160, s[50:51] offset:16
	global_load_dwordx4 v[78:81], v160, s[50:51] offset:2048
	global_load_dwordx4 v[82:85], v160, s[50:51] offset:2064
	global_load_dwordx4 v[86:89], v161, s[50:51]
	global_load_dwordx4 v[90:93], v161, s[50:51] offset:16
	global_load_dwordx4 v[94:97], v161, s[50:51] offset:2048
	global_load_dwordx4 v[98:101], v161, s[50:51] offset:2064
	s_waitcnt vmcnt(0)
	v_pk_mul_f32 v[6:7], v[70:71], v[6:7]
	v_pk_mul_f32 v[8:9], v[72:73], v[8:9]
	v_pk_mul_f32 v[10:11], v[74:75], v[10:11]
	v_pk_mul_f32 v[12:13], v[76:77], v[12:13]
	v_pk_mul_f32 v[14:15], v[78:79], v[14:15]
	v_pk_mul_f32 v[16:17], v[80:81], v[16:17]
	v_pk_mul_f32 v[18:19], v[82:83], v[18:19]
	v_pk_mul_f32 v[20:21], v[84:85], v[20:21]
	v_pk_mul_f32 v[22:23], v[86:87], v[22:23]
	v_pk_mul_f32 v[24:25], v[88:89], v[24:25]
	v_pk_mul_f32 v[26:27], v[90:91], v[26:27]
	v_pk_mul_f32 v[28:29], v[92:93], v[28:29]
	v_pk_mul_f32 v[30:31], v[94:95], v[30:31]
	v_pk_mul_f32 v[32:33], v[96:97], v[32:33]
	v_pk_mul_f32 v[34:35], v[98:99], v[34:35]
	v_pk_mul_f32 v[36:37], v[100:101], v[36:37]
	global_load_dwordx4 v[70:73], v160, s[48:49]
	global_load_dwordx4 v[74:77], v160, s[48:49] offset:16
	global_load_dwordx4 v[78:81], v160, s[48:49] offset:2048
	global_load_dwordx4 v[82:85], v160, s[48:49] offset:2064
	global_load_dwordx4 v[86:89], v161, s[48:49]
	global_load_dwordx4 v[90:93], v161, s[48:49] offset:16
	global_load_dwordx4 v[94:97], v161, s[48:49] offset:2048
	global_load_dwordx4 v[98:101], v161, s[48:49] offset:2064
	s_waitcnt vmcnt(0)
	v_pk_add_f32 v[38:39], v[38:39], v[70:71]
	v_pk_add_f32 v[40:41], v[40:41], v[72:73]
	v_pk_add_f32 v[42:43], v[42:43], v[74:75]
	v_pk_add_f32 v[44:45], v[44:45], v[76:77]
	v_pk_add_f32 v[46:47], v[46:47], v[78:79]
	v_pk_add_f32 v[48:49], v[48:49], v[80:81]
	v_pk_add_f32 v[50:51], v[50:51], v[82:83]
	v_pk_add_f32 v[52:53], v[52:53], v[84:85]
	v_pk_add_f32 v[54:55], v[54:55], v[86:87]
	v_pk_add_f32 v[56:57], v[56:57], v[88:89]
	v_pk_add_f32 v[58:59], v[58:59], v[90:91]
	v_pk_add_f32 v[60:61], v[60:61], v[92:93]
	v_pk_add_f32 v[62:63], v[62:63], v[94:95]
	v_pk_add_f32 v[64:65], v[64:65], v[96:97]
	v_pk_add_f32 v[66:67], v[66:67], v[98:99]
	v_pk_add_f32 v[68:69], v[68:69], v[100:101]
.Lpn_mod_ok_b:
	s_waitcnt vmcnt(10)
	v_cndmask_b32_e64 v136, 0, v135, s[54:55]
	s_nop 1
	v_add_f32_dpp v136, v136, v136 quad_perm:[1,0,3,2] row_mask:0xf bank_mask:0xf bound_ctrl:1
	s_nop 1
	v_add_f32_dpp v136, v136, v136 quad_perm:[2,3,0,1] row_mask:0xf bank_mask:0xf bound_ctrl:1
	s_nop 1
	v_add_f32_dpp v136, v136, v136 row_half_mirror row_mask:0xf bank_mask:0xf bound_ctrl:1
	s_nop 1
	v_add_f32_dpp v136, v136, v136 row_mirror row_mask:0xf bank_mask:0xf bound_ctrl:1
	s_nop 0
	v_readlane_b32 s16, v136, 0
	s_mov_b32 s17, 0x800000
	s_nop 1
	v_mov_b32_e32 v136, s16
	v_fmamk_f32 v136, v136, 0x3a000000, v212
	v_mul_f32_e32 v137, 0x4b800000, v136
	v_cmp_gt_f32_e32 vcc, s17, v136
	s_nop 1
	v_cndmask_b32_e32 v136, v136, v137, vcc
	v_rsq_f32_e32 v136, v136
	s_nop 0
	v_mul_f32_e32 v137, 0x45800000, v136
	v_cndmask_b32_e32 v136, v136, v137, vcc
	v_mov_b32_e32 v137, v136
	v_lshlrev_b32_e32 v70, 16, v118
	v_and_b32_e32 v71, 0xffff0000, v118
	v_lshlrev_b32_e32 v72, 16, v119
	v_and_b32_e32 v73, 0xffff0000, v119
	v_lshlrev_b32_e32 v74, 16, v120
	v_and_b32_e32 v75, 0xffff0000, v120
	v_lshlrev_b32_e32 v76, 16, v121
	v_and_b32_e32 v77, 0xffff0000, v121
	v_lshlrev_b32_e32 v78, 16, v122
	v_and_b32_e32 v79, 0xffff0000, v122
	v_lshlrev_b32_e32 v80, 16, v123
	v_and_b32_e32 v81, 0xffff0000, v123
	v_lshlrev_b32_e32 v82, 16, v124
	v_and_b32_e32 v83, 0xffff0000, v124
	v_lshlrev_b32_e32 v84, 16, v125
	v_and_b32_e32 v85, 0xffff0000, v125
	v_lshlrev_b32_e32 v86, 16, v126
	v_and_b32_e32 v87, 0xffff0000, v126
	v_lshlrev_b32_e32 v88, 16, v127
	v_and_b32_e32 v89, 0xffff0000, v127
	v_lshlrev_b32_e32 v90, 16, v128
	v_and_b32_e32 v91, 0xffff0000, v128
	v_lshlrev_b32_e32 v92, 16, v129
	v_and_b32_e32 v93, 0xffff0000, v129
	v_lshlrev_b32_e32 v94, 16, v130
	v_and_b32_e32 v95, 0xffff0000, v130
	v_lshlrev_b32_e32 v96, 16, v131
	v_and_b32_e32 v97, 0xffff0000, v131
	v_lshlrev_b32_e32 v98, 16, v132
	v_and_b32_e32 v99, 0xffff0000, v132
	v_lshlrev_b32_e32 v100, 16, v133
	v_and_b32_e32 v101, 0xffff0000, v133
	s_add_u32 s18, s12, 2
	s_sub_u32 s19, s13, 1
	s_min_u32 s18, s18, s19
	s_lshl_b32 s16, s18, 12
	s_add_u32 s52, s38, s16
	s_addc_u32 s53, s39, 0
	global_load_dwordx4 v[118:121], v3, s[52:53]
	global_load_dwordx4 v[122:125], v3, s[52:53] offset:1024
	global_load_dwordx4 v[126:129], v3, s[52:53] offset:2048
	global_load_dwordx4 v[130:133], v3, s[52:53] offset:3072
	s_lshl_b32 s16, s18, 2
	s_add_u32 s52, s40, s16
	s_addc_u32 s53, s41, 0
	global_load_dword v135, v162, s[52:53]
	v_pk_mul_f32 v[70:71], v[70:71], v[136:137]
	v_pk_mul_f32 v[72:73], v[72:73], v[136:137]
	v_pk_mul_f32 v[74:75], v[74:75], v[136:137]
	v_pk_mul_f32 v[76:77], v[76:77], v[136:137]
	v_pk_mul_f32 v[78:79], v[78:79], v[136:137]
	v_pk_mul_f32 v[80:81], v[80:81], v[136:137]
	v_pk_mul_f32 v[82:83], v[82:83], v[136:137]
	v_pk_mul_f32 v[84:85], v[84:85], v[136:137]
	v_pk_mul_f32 v[86:87], v[86:87], v[136:137]
	v_pk_mul_f32 v[88:89], v[88:89], v[136:137]
	v_pk_mul_f32 v[90:91], v[90:91], v[136:137]
	v_pk_mul_f32 v[92:93], v[92:93], v[136:137]
	v_pk_mul_f32 v[94:95], v[94:95], v[136:137]
	v_pk_mul_f32 v[96:97], v[96:97], v[136:137]
	v_pk_mul_f32 v[98:99], v[98:99], v[136:137]
	v_pk_mul_f32 v[100:101], v[100:101], v[136:137]
	v_pk_fma_f32 v[70:71], v[70:71], v[6:7], v[38:39]
	v_pk_fma_f32 v[72:73], v[72:73], v[8:9], v[40:41]
	v_pk_fma_f32 v[74:75], v[74:75], v[10:11], v[42:43]
	v_pk_fma_f32 v[76:77], v[76:77], v[12:13], v[44:45]
	v_pk_fma_f32 v[78:79], v[78:79], v[14:15], v[46:47]
	v_pk_fma_f32 v[80:81], v[80:81], v[16:17], v[48:49]
	v_pk_fma_f32 v[82:83], v[82:83], v[18:19], v[50:51]
	v_pk_fma_f32 v[84:85], v[84:85], v[20:21], v[52:53]
	v_pk_fma_f32 v[86:87], v[86:87], v[22:23], v[54:55]
	v_pk_fma_f32 v[88:89], v[88:89], v[24:25], v[56:57]
	v_pk_fma_f32 v[90:91], v[90:91], v[26:27], v[58:59]
	v_pk_fma_f32 v[92:93], v[92:93], v[28:29], v[60:61]
	v_pk_fma_f32 v[94:95], v[94:95], v[30:31], v[62:63]
	v_pk_fma_f32 v[96:97], v[96:97], v[32:33], v[64:65]
	v_pk_fma_f32 v[98:99], v[98:99], v[34:35], v[66:67]
	v_pk_fma_f32 v[100:101], v[100:101], v[36:37], v[68:69]
	s_cmp_lg_u32 s14, 0
	s_cbranch_scc1 .Lpn_out_b
	v_max3_f32 v138, |v70|, |v71|, |v72|
	v_max3_f32 v139, |v74|, |v75|, |v76|
	v_max3_f32 v140, |v78|, |v79|, |v80|
	v_max3_f32 v141, |v82|, |v83|, |v84|
	v_max3_f32 v142, |v86|, |v87|, |v88|
	v_max3_f32 v143, |v90|, |v91|, |v92|
	v_max3_f32 v144, |v94|, |v95|, |v96|
	v_max3_f32 v145, |v98|, |v99|, |v100|
	v_max_f32_e64 v138, v138, |v73|
	v_max_f32_e64 v139, v139, |v77|
	v_max_f32_e64 v140, v140, |v81|
	v_max_f32_e64 v141, v141, |v85|
	v_max_f32_e64 v142, v142, |v89|
	v_max_f32_e64 v143, v143, |v93|
	v_max_f32_e64 v144, v144, |v97|
	v_max_f32_e64 v145, v145, |v101|
	v_max3_f32 v138, v138, v139, v140
	v_max3_f32 v141, v141, v142, v143
	v_max3_f32 v138, v138, v141, v144
	v_max_f32_e32 v138, v138, v145
	s_nop 1
	v_mov_b32_dpp v139, v138 quad_perm:[1,0,3,2] row_mask:0xf bank_mask:0xf bound_ctrl:1
	v_max_f32_e32 v138, v138, v139
	s_nop 1
	v_mov_b32_dpp v139, v138 quad_perm:[2,3,0,1] row_mask:0xf bank_mask:0xf bound_ctrl:1
	v_max_f32_e32 v138, v138, v139
	s_nop 1
	v_mov_b32_dpp v139, v138 row_half_mirror row_mask:0xf bank_mask:0xf bound_ctrl:1
	v_max_f32_e32 v138, v138, v139
	s_nop 1
	v_mov_b32_dpp v139, v138 row_mirror row_mask:0xf bank_mask:0xf bound_ctrl:1
	v_max_f32_e32 v138, v138, v139
	v_mov_b32_e32 v139, v138
	s_nop 1
	v_permlane16_swap_b32_e32 v138, v139
	v_max_f32_e32 v138, v138, v139
	v_mov_b32_e32 v139, v138
	s_nop 1
	v_permlane32_swap_b32_e32 v138, v139
	v_max_f32_e32 v138, v138, v139
	v_div_scale_f32 v140, s[100:101], v138, v138, s95
	v_rcp_f32_e32 v142, v140
	v_div_scale_f32 v141, vcc, s95, v138, s95
	v_fma_f32 v143, -v140, v142, 1.0
	v_fmac_f32_e32 v142, v143, v142
	v_mul_f32_e32 v143, v141, v142
	v_fma_f32 v144, -v140, v143, v141
	v_fmac_f32_e32 v143, v144, v142
	v_fma_f32 v140, -v140, v143, v141
	v_div_fmas_f32 v140, v140, v142, v143
	v_div_fixup_f32 v140, v140, v138, s95
	v_cmp_lt_f32_e32 vcc, 0, v138
	v_mul_f32_e32 v141, 0x3b124925, v138
	v_mov_b32_e32 v143, 0
	v_cndmask_b32_e32 v142, 0, v140, vcc
	s_lshl_b32 s16, s12, 2
	s_add_u32 s52, s44, s16
	s_addc_u32 s53, s45, 0
	s_mov_b64 exec, 1
	global_store_dword v143, v141, s[52:53]
	s_mov_b64 exec, -1
	v_pk_mul_f32 v[70:71], v[70:71], v[142:143] op_sel_hi:[1,0]
	v_pk_mul_f32 v[72:73], v[72:73], v[142:143] op_sel_hi:[1,0]
	v_pk_mul_f32 v[74:75], v[74:75], v[142:143] op_sel_hi:[1,0]
	v_pk_mul_f32 v[76:77], v[76:77], v[142:143] op_sel_hi:[1,0]
	v_pk_mul_f32 v[78:79], v[78:79], v[142:143] op_sel_hi:[1,0]
	v_pk_mul_f32 v[80:81], v[80:81], v[142:143] op_sel_hi:[1,0]
	v_pk_mul_f32 v[82:83], v[82:83], v[142:143] op_sel_hi:[1,0]
	v_pk_mul_f32 v[84:85], v[84:85], v[142:143] op_sel_hi:[1,0]
	v_pk_mul_f32 v[86:87], v[86:87], v[142:143] op_sel_hi:[1,0]
	v_pk_mul_f32 v[88:89], v[88:89], v[142:143] op_sel_hi:[1,0]
	v_pk_mul_f32 v[90:91], v[90:91], v[142:143] op_sel_hi:[1,0]
	v_pk_mul_f32 v[92:93], v[92:93], v[142:143] op_sel_hi:[1,0]
	v_pk_mul_f32 v[94:95], v[94:95], v[142:143] op_sel_hi:[1,0]
	v_pk_mul_f32 v[96:97], v[96:97], v[142:143] op_sel_hi:[1,0]
	v_pk_mul_f32 v[98:99], v[98:99], v[142:143] op_sel_hi:[1,0]
	v_pk_mul_f32 v[100:101], v[100:101], v[142:143] op_sel_hi:[1,0]
	v_mov_b32_e32 v146, 0
	v_mov_b32_e32 v147, 0
	v_mov_b32_e32 v148, 0
	v_mov_b32_e32 v149, 0
	v_mov_b32_e32 v150, 0
	v_mov_b32_e32 v151, 0
	v_mov_b32_e32 v152, 0
	v_mov_b32_e32 v153, 0
	v_cvt_pk_fp8_f32 v146, v70, v71
	v_cvt_pk_fp8_f32 v147, v74, v75
	v_cvt_pk_fp8_f32 v148, v78, v79
	v_cvt_pk_fp8_f32 v149, v82, v83
	v_cvt_pk_fp8_f32 v150, v86, v87
	v_cvt_pk_fp8_f32 v151, v90, v91
	v_cvt_pk_fp8_f32 v152, v94, v95
	v_cvt_pk_fp8_f32 v153, v98, v99
	v_cvt_pk_fp8_f32 v146, v72, v73 op_sel:[0,0,1]
	v_cvt_pk_fp8_f32 v147, v76, v77 op_sel:[0,0,1]
	v_cvt_pk_fp8_f32 v148, v80, v81 op_sel:[0,0,1]
	v_cvt_pk_fp8_f32 v149, v84, v85 op_sel:[0,0,1]
	v_cvt_pk_fp8_f32 v150, v88, v89 op_sel:[0,0,1]
	v_cvt_pk_fp8_f32 v151, v92, v93 op_sel:[0,0,1]
	v_cvt_pk_fp8_f32 v152, v96, v97 op_sel:[0,0,1]
	v_cvt_pk_fp8_f32 v153, v100, v101 op_sel:[0,0,1]
	s_lshl_b32 s16, s12, 11
	s_add_u32 s52, s42, s16
	s_addc_u32 s53, s43, 0
	global_store_dwordx2 v163, v[146:147], s[52:53]
	global_store_dwordx2 v163, v[148:149], s[52:53] offset:512
	global_store_dwordx2 v163, v[150:151], s[52:53] offset:1024
	global_store_dwordx2 v163, v[152:153], s[52:53] offset:1536
	s_branch .Lpn_next_b

.Lpn_next_b:
	s_add_u32 s12, s12, 1
	s_cmp_ge_u32 s12, s13
	s_cbranch_scc1 .Lpn_end
	s_cmp_lg_u32 s14, 0
	s_cbranch_scc1 .Lpn_mod_ok_c
	s_lshr_b32 s16, s12, 12
	s_cmp_lt_u32 s12, 0x4000
	s_cselect_b32 s16, s16, 4
	s_cmp_eq_u32 s16, s15
	s_cbranch_scc1 .Lpn_mod_ok_c
	s_mov_b32 s15, s16
	s_mul_i32 s16, s16, 0xc000
	s_add_u32 s52, s46, s16
	s_addc_u32 s53, s47, 0
	s_add_u32 s10, s52, 0x2000
	s_addc_u32 s11, s53, 0
	s_add_u32 s16, s48, 0x2000
	s_addc_u32 s17, s49, 0
	global_load_dwordx4 v[6:9], v160, s[10:11]
	global_load_dwordx4 v[70:73], v160, s[16:17]
	global_load_dwordx4 v[38:41], v160, s[52:53]
	global_load_dwordx4 v[10:13], v160, s[10:11] offset:16
	global_load_dwordx4 v[74:77], v160, s[16:17] offset:16
	global_load_dwordx4 v[42:45], v160, s[52:53] offset:16
	global_load_dwordx4 v[14:17], v160, s[10:11] offset:2048
	global_load_dwordx4 v[78:81], v160, s[16:17] offset:2048
	global_load_dwordx4 v[46:49], v160, s[52:53] offset:2048
	global_load_dwordx4 v[18:21], v160, s[10:11] offset:2064
	global_load_dwordx4 v[82:85], v160, s[16:17] offset:2064
	global_load_dwordx4 v[50:53], v160, s[52:53] offset:2064
	global_load_dwordx4 v[22:25], v161, s[10:11]
	global_load_dwordx4 v[86:89], v161, s[16:17]
	global_load_dwordx4 v[54:57], v161, s[52:53]
	global_load_dwordx4 v[26:29], v161, s[10:11] offset:16
	global_load_dwordx4 v[90:93], v161, s[16:17] offset:16
	global_load_dwordx4 v[58:61], v161, s[52:53] offset:16
	global_load_dwordx4 v[30:33], v161, s[10:11] offset:2048
	global_load_dwordx4 v[94:97], v161, s[16:17] offset:2048
	global_load_dwordx4 v[62:65], v161, s[52:53] offset:2048
	global_load_dwordx4 v[34:37], v161, s[10:11] offset:2064
	global_load_dwordx4 v[98:101], v161, s[16:17] offset:2064
	global_load_dwordx4 v[66:69], v161, s[52:53] offset:2064
	s_waitcnt vmcnt(0)
	v_pk_add_f32 v[6:7], v[6:7], v[70:71]
	v_pk_add_f32 v[6:7], v[6:7], 1.0 op_sel_hi:[1,0]
	v_pk_add_f32 v[8:9], v[8:9], v[72:73]
	v_pk_add_f32 v[8:9], v[8:9], 1.0 op_sel_hi:[1,0]
	v_pk_add_f32 v[10:11], v[10:11], v[74:75]
	v_pk_add_f32 v[10:11], v[10:11], 1.0 op_sel_hi:[1,0]
	v_pk_add_f32 v[12:13], v[12:13], v[76:77]
	v_pk_add_f32 v[12:13], v[12:13], 1.0 op_sel_hi:[1,0]
	v_pk_add_f32 v[14:15], v[14:15], v[78:79]
	v_pk_add_f32 v[14:15], v[14:15], 1.0 op_sel_hi:[1,0]
	v_pk_add_f32 v[16:17], v[16:17], v[80:81]
	v_pk_add_f32 v[16:17], v[16:17], 1.0 op_sel_hi:[1,0]
	v_pk_add_f32 v[18:19], v[18:19], v[82:83]
	v_pk_add_f32 v[18:19], v[18:19], 1.0 op_sel_hi:[1,0]
	v_pk_add_f32 v[20:21], v[20:21], v[84:85]
	v_pk_add_f32 v[20:21], v[20:21], 1.0 op_sel_hi:[1,0]
	v_pk_add_f32 v[22:23], v[22:23], v[86:87]
	v_pk_add_f32 v[22:23], v[22:23], 1.0 op_sel_hi:[1,0]
	v_pk_add_f32 v[24:25], v[24:25], v[88:89]
	v_pk_add_f32 v[24:25], v[24:25], 1.0 op_sel_hi:[1,0]
	v_pk_add_f32 v[26:27], v[26:27], v[90:91]
	v_pk_add_f32 v[26:27], v[26:27], 1.0 op_sel_hi:[1,0]
	v_pk_add_f32 v[28:29], v[28:29], v[92:93]
	v_pk_add_f32 v[28:29], v[28:29], 1.0 op_sel_hi:[1,0]
	v_pk_add_f32 v[30:31], v[30:31], v[94:95]
	v_pk_add_f32 v[30:31], v[30:31], 1.0 op_sel_hi:[1,0]
	v_pk_add_f32 v[32:33], v[32:33], v[96:97]
	v_pk_add_f32 v[32:33], v[32:33], 1.0 op_sel_hi:[1,0]
	v_pk_add_f32 v[34:35], v[34:35], v[98:99]
	v_pk_add_f32 v[34:35], v[34:35], 1.0 op_sel_hi:[1,0]
	v_pk_add_f32 v[36:37], v[36:37], v[100:101]
	v_pk_add_f32 v[36:37], v[36:37], 1.0 op_sel_hi:[1,0]
	global_load_dwordx4 v[70:73], v160, s[50:51]
	global_load_dwordx4 v[74:77], v160, s[50:51] offset:16
	global_load_dwordx4 v[78:81], v160, s[50:51] offset:2048
	global_load_dwordx4 v[82:85], v160, s[50:51] offset:2064
	global_load_dwordx4 v[86:89], v161, s[50:51]
	global_load_dwordx4 v[90:93], v161, s[50:51] offset:16
	global_load_dwordx4 v[94:97], v161, s[50:51] offset:2048
	global_load_dwordx4 v[98:101], v161, s[50:51] offset:2064
	s_waitcnt vmcnt(0)
	v_pk_mul_f32 v[6:7], v[70:71], v[6:7]
	v_pk_mul_f32 v[8:9], v[72:73], v[8:9]
	v_pk_mul_f32 v[10:11], v[74:75], v[10:11]
	v_pk_mul_f32 v[12:13], v[76:77], v[12:13]
	v_pk_mul_f32 v[14:15], v[78:79], v[14:15]
	v_pk_mul_f32 v[16:17], v[80:81], v[16:17]
	v_pk_mul_f32 v[18:19], v[82:83], v[18:19]
	v_pk_mul_f32 v[20:21], v[84:85], v[20:21]
	v_pk_mul_f32 v[22:23], v[86:87], v[22:23]
	v_pk_mul_f32 v[24:25], v[88:89], v[24:25]
	v_pk_mul_f32 v[26:27], v[90:91], v[26:27]
	v_pk_mul_f32 v[28:29], v[92:93], v[28:29]
	v_pk_mul_f32 v[30:31], v[94:95], v[30:31]
	v_pk_mul_f32 v[32:33], v[96:97], v[32:33]
	v_pk_mul_f32 v[34:35], v[98:99], v[34:35]
	v_pk_mul_f32 v[36:37], v[100:101], v[36:37]
	global_load_dwordx4 v[70:73], v160, s[48:49]
	global_load_dwordx4 v[74:77], v160, s[48:49] offset:16
	global_load_dwordx4 v[78:81], v160, s[48:49] offset:2048
	global_load_dwordx4 v[82:85], v160, s[48:49] offset:2064
	global_load_dwordx4 v[86:89], v161, s[48:49]
	global_load_dwordx4 v[90:93], v161, s[48:49] offset:16
	global_load_dwordx4 v[94:97], v161, s[48:49] offset:2048
	global_load_dwordx4 v[98:101], v161, s[48:49] offset:2064
	s_waitcnt vmcnt(0)
	v_pk_add_f32 v[38:39], v[38:39], v[70:71]
	v_pk_add_f32 v[40:41], v[40:41], v[72:73]
	v_pk_add_f32 v[42:43], v[42:43], v[74:75]
	v_pk_add_f32 v[44:45], v[44:45], v[76:77]
	v_pk_add_f32 v[46:47], v[46:47], v[78:79]
	v_pk_add_f32 v[48:49], v[48:49], v[80:81]
	v_pk_add_f32 v[50:51], v[50:51], v[82:83]
	v_pk_add_f32 v[52:53], v[52:53], v[84:85]
	v_pk_add_f32 v[54:55], v[54:55], v[86:87]
	v_pk_add_f32 v[56:57], v[56:57], v[88:89]
	v_pk_add_f32 v[58:59], v[58:59], v[90:91]
	v_pk_add_f32 v[60:61], v[60:61], v[92:93]
	v_pk_add_f32 v[62:63], v[62:63], v[94:95]
	v_pk_add_f32 v[64:65], v[64:65], v[96:97]
	v_pk_add_f32 v[66:67], v[66:67], v[98:99]
	v_pk_add_f32 v[68:69], v[68:69], v[100:101]
.Lpn_mod_ok_c:
	s_waitcnt vmcnt(10)
	v_cndmask_b32_e64 v136, 0, v134, s[54:55]
	s_nop 1
	v_add_f32_dpp v136, v136, v136 quad_perm:[1,0,3,2] row_mask:0xf bank_mask:0xf bound_ctrl:1
	s_nop 1
	v_add_f32_dpp v136, v136, v136 quad_perm:[2,3,0,1] row_mask:0xf bank_mask:0xf bound_ctrl:1
	s_nop 1
	v_add_f32_dpp v136, v136, v136 row_half_mirror row_mask:0xf bank_mask:0xf bound_ctrl:1
	s_nop 1
	v_add_f32_dpp v136, v136, v136 row_mirror row_mask:0xf bank_mask:0xf bound_ctrl:1
	s_nop 0
	v_readlane_b32 s16, v136, 0
	s_mov_b32 s17, 0x800000
	s_nop 1
	v_mov_b32_e32 v136, s16
	v_fmamk_f32 v136, v136, 0x3a000000, v212
	v_mul_f32_e32 v137, 0x4b800000, v136
	v_cmp_gt_f32_e32 vcc, s17, v136
	s_nop 1
	v_cndmask_b32_e32 v136, v136, v137, vcc
	v_rsq_f32_e32 v136, v136
	s_nop 0
	v_mul_f32_e32 v137, 0x45800000, v136
	v_cndmask_b32_e32 v136, v136, v137, vcc
	v_mov_b32_e32 v137, v136
	v_lshlrev_b32_e32 v70, 16, v102
	v_and_b32_e32 v71, 0xffff0000, v102
	v_lshlrev_b32_e32 v72, 16, v103
	v_and_b32_e32 v73, 0xffff0000, v103
	v_lshlrev_b32_e32 v74, 16, v104
	v_and_b32_e32 v75, 0xffff0000, v104
	v_lshlrev_b32_e32 v76, 16, v105
	v_and_b32_e32 v77, 0xffff0000, v105
	v_lshlrev_b32_e32 v78, 16, v106
	v_and_b32_e32 v79, 0xffff0000, v106
	v_lshlrev_b32_e32 v80, 16, v107
	v_and_b32_e32 v81, 0xffff0000, v107
	v_lshlrev_b32_e32 v82, 16, v108
	v_and_b32_e32 v83, 0xffff0000, v108
	v_lshlrev_b32_e32 v84, 16, v109
	v_and_b32_e32 v85, 0xffff0000, v109
	v_lshlrev_b32_e32 v86, 16, v110
	v_and_b32_e32 v87, 0xffff0000, v110
	v_lshlrev_b32_e32 v88, 16, v111
	v_and_b32_e32 v89, 0xffff0000, v111
	v_lshlrev_b32_e32 v90, 16, v112
	v_and_b32_e32 v91, 0xffff0000, v112
	v_lshlrev_b32_e32 v92, 16, v113
	v_and_b32_e32 v93, 0xffff0000, v113
	v_lshlrev_b32_e32 v94, 16, v114
	v_and_b32_e32 v95, 0xffff0000, v114
	v_lshlrev_b32_e32 v96, 16, v115
	v_and_b32_e32 v97, 0xffff0000, v115
	v_lshlrev_b32_e32 v98, 16, v116
	v_and_b32_e32 v99, 0xffff0000, v116
	v_lshlrev_b32_e32 v100, 16, v117
	v_and_b32_e32 v101, 0xffff0000, v117
	s_add_u32 s18, s12, 2
	s_sub_u32 s19, s13, 1
	s_min_u32 s18, s18, s19
	s_lshl_b32 s16, s18, 12
	s_add_u32 s52, s38, s16
	s_addc_u32 s53, s39, 0
	global_load_dwordx4 v[102:105], v3, s[52:53]
	global_load_dwordx4 v[106:109], v3, s[52:53] offset:1024
	global_load_dwordx4 v[110:113], v3, s[52:53] offset:2048
	global_load_dwordx4 v[114:117], v3, s[52:53] offset:3072
	s_lshl_b32 s16, s18, 2
	s_add_u32 s52, s40, s16
	s_addc_u32 s53, s41, 0
	global_load_dword v134, v162, s[52:53]
	v_pk_mul_f32 v[70:71], v[70:71], v[136:137]
	v_pk_mul_f32 v[72:73], v[72:73], v[136:137]
	v_pk_mul_f32 v[74:75], v[74:75], v[136:137]
	v_pk_mul_f32 v[76:77], v[76:77], v[136:137]
	v_pk_mul_f32 v[78:79], v[78:79], v[136:137]
	v_pk_mul_f32 v[80:81], v[80:81], v[136:137]
	v_pk_mul_f32 v[82:83], v[82:83], v[136:137]
	v_pk_mul_f32 v[84:85], v[84:85], v[136:137]
	v_pk_mul_f32 v[86:87], v[86:87], v[136:137]
	v_pk_mul_f32 v[88:89], v[88:89], v[136:137]
	v_pk_mul_f32 v[90:91], v[90:91], v[136:137]
	v_pk_mul_f32 v[92:93], v[92:93], v[136:137]
	v_pk_mul_f32 v[94:95], v[94:95], v[136:137]
	v_pk_mul_f32 v[96:97], v[96:97], v[136:137]
	v_pk_mul_f32 v[98:99], v[98:99], v[136:137]
	v_pk_mul_f32 v[100:101], v[100:101], v[136:137]
	v_pk_fma_f32 v[70:71], v[70:71], v[6:7], v[38:39]
	v_pk_fma_f32 v[72:73], v[72:73], v[8:9], v[40:41]
	v_pk_fma_f32 v[74:75], v[74:75], v[10:11], v[42:43]
	v_pk_fma_f32 v[76:77], v[76:77], v[12:13], v[44:45]
	v_pk_fma_f32 v[78:79], v[78:79], v[14:15], v[46:47]
	v_pk_fma_f32 v[80:81], v[80:81], v[16:17], v[48:49]
	v_pk_fma_f32 v[82:83], v[82:83], v[18:19], v[50:51]
	v_pk_fma_f32 v[84:85], v[84:85], v[20:21], v[52:53]
	v_pk_fma_f32 v[86:87], v[86:87], v[22:23], v[54:55]
	v_pk_fma_f32 v[88:89], v[88:89], v[24:25], v[56:57]
	v_pk_fma_f32 v[90:91], v[90:91], v[26:27], v[58:59]
	v_pk_fma_f32 v[92:93], v[92:93], v[28:29], v[60:61]
	v_pk_fma_f32 v[94:95], v[94:95], v[30:31], v[62:63]
	v_pk_fma_f32 v[96:97], v[96:97], v[32:33], v[64:65]
	v_pk_fma_f32 v[98:99], v[98:99], v[34:35], v[66:67]
	v_pk_fma_f32 v[100:101], v[100:101], v[36:37], v[68:69]
	s_cmp_lg_u32 s14, 0
	s_cbranch_scc1 .Lpn_out_c
	v_max3_f32 v138, |v70|, |v71|, |v72|
	v_max3_f32 v139, |v74|, |v75|, |v76|
	v_max3_f32 v140, |v78|, |v79|, |v80|
	v_max3_f32 v141, |v82|, |v83|, |v84|
	v_max3_f32 v142, |v86|, |v87|, |v88|
	v_max3_f32 v143, |v90|, |v91|, |v92|
	v_max3_f32 v144, |v94|, |v95|, |v96|
	v_max3_f32 v145, |v98|, |v99|, |v100|
	v_max_f32_e64 v138, v138, |v73|
	v_max_f32_e64 v139, v139, |v77|
	v_max_f32_e64 v140, v140, |v81|
	v_max_f32_e64 v141, v141, |v85|
	v_max_f32_e64 v142, v142, |v89|
	v_max_f32_e64 v143, v143, |v93|
	v_max_f32_e64 v144, v144, |v97|
	v_max_f32_e64 v145, v145, |v101|
	v_max3_f32 v138, v138, v139, v140
	v_max3_f32 v141, v141, v142, v143
	v_max3_f32 v138, v138, v141, v144
	v_max_f32_e32 v138, v138, v145
	s_nop 1
	v_mov_b32_dpp v139, v138 quad_perm:[1,0,3,2] row_mask:0xf bank_mask:0xf bound_ctrl:1
	v_max_f32_e32 v138, v138, v139
	s_nop 1
	v_mov_b32_dpp v139, v138 quad_perm:[2,3,0,1] row_mask:0xf bank_mask:0xf bound_ctrl:1
	v_max_f32_e32 v138, v138, v139
	s_nop 1
	v_mov_b32_dpp v139, v138 row_half_mirror row_mask:0xf bank_mask:0xf bound_ctrl:1
	v_max_f32_e32 v138, v138, v139
	s_nop 1
	v_mov_b32_dpp v139, v138 row_mirror row_mask:0xf bank_mask:0xf bound_ctrl:1
	v_max_f32_e32 v138, v138, v139
	v_mov_b32_e32 v139, v138
	s_nop 1
	v_permlane16_swap_b32_e32 v138, v139
	v_max_f32_e32 v138, v138, v139
	v_mov_b32_e32 v139, v138
	s_nop 1
	v_permlane32_swap_b32_e32 v138, v139
	v_max_f32_e32 v138, v138, v139
	v_div_scale_f32 v140, s[100:101], v138, v138, s95
	v_rcp_f32_e32 v142, v140
	v_div_scale_f32 v141, vcc, s95, v138, s95
	v_fma_f32 v143, -v140, v142, 1.0
	v_fmac_f32_e32 v142, v143, v142
	v_mul_f32_e32 v143, v141, v142
	v_fma_f32 v144, -v140, v143, v141
	v_fmac_f32_e32 v143, v144, v142
	v_fma_f32 v140, -v140, v143, v141
	v_div_fmas_f32 v140, v140, v142, v143
	v_div_fixup_f32 v140, v140, v138, s95
	v_cmp_lt_f32_e32 vcc, 0, v138
	v_mul_f32_e32 v141, 0x3b124925, v138
	v_mov_b32_e32 v143, 0
	v_cndmask_b32_e32 v142, 0, v140, vcc
	s_lshl_b32 s16, s12, 2
	s_add_u32 s52, s44, s16
	s_addc_u32 s53, s45, 0
	s_mov_b64 exec, 1
	global_store_dword v143, v141, s[52:53]
	s_mov_b64 exec, -1
	v_pk_mul_f32 v[70:71], v[70:71], v[142:143] op_sel_hi:[1,0]
	v_pk_mul_f32 v[72:73], v[72:73], v[142:143] op_sel_hi:[1,0]
	v_pk_mul_f32 v[74:75], v[74:75], v[142:143] op_sel_hi:[1,0]
	v_pk_mul_f32 v[76:77], v[76:77], v[142:143] op_sel_hi:[1,0]
	v_pk_mul_f32 v[78:79], v[78:79], v[142:143] op_sel_hi:[1,0]
	v_pk_mul_f32 v[80:81], v[80:81], v[142:143] op_sel_hi:[1,0]
	v_pk_mul_f32 v[82:83], v[82:83], v[142:143] op_sel_hi:[1,0]
	v_pk_mul_f32 v[84:85], v[84:85], v[142:143] op_sel_hi:[1,0]
	v_pk_mul_f32 v[86:87], v[86:87], v[142:143] op_sel_hi:[1,0]
	v_pk_mul_f32 v[88:89], v[88:89], v[142:143] op_sel_hi:[1,0]
	v_pk_mul_f32 v[90:91], v[90:91], v[142:143] op_sel_hi:[1,0]
	v_pk_mul_f32 v[92:93], v[92:93], v[142:143] op_sel_hi:[1,0]
	v_pk_mul_f32 v[94:95], v[94:95], v[142:143] op_sel_hi:[1,0]
	v_pk_mul_f32 v[96:97], v[96:97], v[142:143] op_sel_hi:[1,0]
	v_pk_mul_f32 v[98:99], v[98:99], v[142:143] op_sel_hi:[1,0]
	v_pk_mul_f32 v[100:101], v[100:101], v[142:143] op_sel_hi:[1,0]
	v_mov_b32_e32 v146, 0
	v_mov_b32_e32 v147, 0
	v_mov_b32_e32 v148, 0
	v_mov_b32_e32 v149, 0
	v_mov_b32_e32 v150, 0
	v_mov_b32_e32 v151, 0
	v_mov_b32_e32 v152, 0
	v_mov_b32_e32 v153, 0
	v_cvt_pk_fp8_f32 v146, v70, v71
	v_cvt_pk_fp8_f32 v147, v74, v75
	v_cvt_pk_fp8_f32 v148, v78, v79
	v_cvt_pk_fp8_f32 v149, v82, v83
	v_cvt_pk_fp8_f32 v150, v86, v87
	v_cvt_pk_fp8_f32 v151, v90, v91
	v_cvt_pk_fp8_f32 v152, v94, v95
	v_cvt_pk_fp8_f32 v153, v98, v99
	v_cvt_pk_fp8_f32 v146, v72, v73 op_sel:[0,0,1]
	v_cvt_pk_fp8_f32 v147, v76, v77 op_sel:[0,0,1]
	v_cvt_pk_fp8_f32 v148, v80, v81 op_sel:[0,0,1]
	v_cvt_pk_fp8_f32 v149, v84, v85 op_sel:[0,0,1]
	v_cvt_pk_fp8_f32 v150, v88, v89 op_sel:[0,0,1]
	v_cvt_pk_fp8_f32 v151, v92, v93 op_sel:[0,0,1]
	v_cvt_pk_fp8_f32 v152, v96, v97 op_sel:[0,0,1]
	v_cvt_pk_fp8_f32 v153, v100, v101 op_sel:[0,0,1]
	s_lshl_b32 s16, s12, 11
	s_add_u32 s52, s42, s16
	s_addc_u32 s53, s43, 0
	global_store_dwordx2 v163, v[146:147], s[52:53]
	global_store_dwordx2 v163, v[148:149], s[52:53] offset:512
	global_store_dwordx2 v163, v[150:151], s[52:53] offset:1024
	global_store_dwordx2 v163, v[152:153], s[52:53] offset:1536
	s_branch .Lpn_next_c

.Lpn_next_c:
	s_add_u32 s12, s12, 1
	s_cmp_ge_u32 s12, s13
	s_cbranch_scc1 .Lpn_end
	s_branch .Lpn_loop
.Lpn_end:
.LBB0_1329:
	v_readlane_b32 s4, v255, 37
	v_readlane_b32 s5, v255, 38
	s_and_b64 s[6:7], s[4:5], s[6:7]
	v_readlane_b32 s4, v254, 31
	v_readlane_b32 s5, v254, 32
	s_and_b64 s[8:9], s[8:9], s[4:5]
	s_and_b64 s[6:7], s[6:7], s[8:9]
	s_andn2_b64 vcc, exec, s[6:7]
	s_cbranch_vccz .LBB0_1330
	s_getpc_b64 s[98:99]
